# balanced DMA + nt on the in-proj epilogue QKV stores
# speedup vs baseline: 1.0071x; 1.0018x over previous
.LBB0_246:
	s_lshl_b32 s29, s38, 8
	s_lshl_b32 s38, s34, 1
	s_ashr_i32 s39, s38, 31
	s_lshl_b64 s[34:35], s[38:39], 22
	v_readlane_b32 s44, v254, 14
	v_readlane_b32 s45, v254, 15
	s_add_u32 s34, s44, s34
	s_addc_u32 s35, s45, s35
	s_or_b32 s38, s38, 1
	v_add_u32_e32 v0, s29, v171
	s_ashr_i32 s39, s38, 31
	v_ashrrev_i32_e32 v1, 31, v0
	s_lshl_b64 s[38:39], s[38:39], 22
	v_lshlrev_b64 v[4:5], 8, v[0:1]
	s_add_u32 s38, s44, s38
	v_lshl_add_u64 v[6:7], s[34:35], 0, v[4:5]
	s_addc_u32 s39, s45, s39
	v_lshl_add_u64 v[6:7], v[6:7], 0, s[16:17]
	v_lshl_add_u64 v[4:5], s[38:39], 0, v[4:5]
	v_cvt_pk_bf16_f32 v0, v156, v157
	v_lshl_add_u64 v[6:7], v[6:7], 0, v[168:169]
	v_lshl_add_u64 v[4:5], v[4:5], 0, s[16:17]
	v_cvt_pk_bf16_f32 v1, v158, v159
	v_cvt_pk_bf16_f32 v2, v152, v153
	v_cvt_pk_bf16_f32 v3, v154, v155
	global_store_dwordx4 v[6:7], v[0:3], off nt
	v_lshl_add_u64 v[4:5], v[4:5], 0, v[168:169]
	s_andn2_b64 vcc, exec, s[42:43]
	v_cvt_pk_bf16_f32 v0, v178, v179
	v_cvt_pk_bf16_f32 v1, v126, v127
	v_cvt_pk_bf16_f32 v2, v180, v181
	v_cvt_pk_bf16_f32 v3, v124, v125
	global_store_dwordx4 v[4:5], v[0:3], off nt
	s_nop 1
	v_or_b32_e32 v0, 16, v171
	v_add_u32_e32 v0, s29, v0
	v_ashrrev_i32_e32 v1, 31, v0
	v_lshlrev_b64 v[4:5], 8, v[0:1]
	v_lshl_add_u64 v[6:7], s[34:35], 0, v[4:5]
	v_lshl_add_u64 v[6:7], v[6:7], 0, s[16:17]
	v_lshl_add_u64 v[4:5], s[38:39], 0, v[4:5]
	v_cvt_pk_bf16_f32 v0, v148, v149
	v_lshl_add_u64 v[6:7], v[6:7], 0, v[168:169]
	v_lshl_add_u64 v[4:5], v[4:5], 0, s[16:17]
	v_cvt_pk_bf16_f32 v1, v150, v151
	v_cvt_pk_bf16_f32 v2, v144, v145
	v_cvt_pk_bf16_f32 v3, v146, v147
	global_store_dwordx4 v[6:7], v[0:3], off nt
	v_lshl_add_u64 v[4:5], v[4:5], 0, v[168:169]
	s_nop 0
	v_cvt_pk_bf16_f32 v0, v120, v121
	v_cvt_pk_bf16_f32 v1, v118, v119
	v_cvt_pk_bf16_f32 v2, v122, v123
	v_cvt_pk_bf16_f32 v3, v116, v117
	global_store_dwordx4 v[4:5], v[0:3], off nt
	s_nop 1
	v_or_b32_e32 v0, 32, v171
	v_add_u32_e32 v0, s29, v0
	v_ashrrev_i32_e32 v1, 31, v0
	v_lshlrev_b64 v[4:5], 8, v[0:1]
	v_lshl_add_u64 v[6:7], s[34:35], 0, v[4:5]
	v_lshl_add_u64 v[6:7], v[6:7], 0, s[16:17]
	v_lshl_add_u64 v[4:5], s[38:39], 0, v[4:5]
	v_cvt_pk_bf16_f32 v0, v140, v141
	v_lshl_add_u64 v[6:7], v[6:7], 0, v[168:169]
	v_lshl_add_u64 v[4:5], v[4:5], 0, s[16:17]
	v_cvt_pk_bf16_f32 v1, v142, v143
	v_cvt_pk_bf16_f32 v2, v136, v137
	v_cvt_pk_bf16_f32 v3, v138, v139
	global_store_dwordx4 v[6:7], v[0:3], off nt
	v_lshl_add_u64 v[4:5], v[4:5], 0, v[168:169]
	s_nop 0
	v_cvt_pk_bf16_f32 v0, v108, v109
	v_cvt_pk_bf16_f32 v1, v110, v111
	v_cvt_pk_bf16_f32 v2, v112, v113
	v_cvt_pk_bf16_f32 v3, v106, v107
	global_store_dwordx4 v[4:5], v[0:3], off nt
	s_nop 1
	v_or_b32_e32 v0, 48, v171
	v_add_u32_e32 v0, s29, v0
	v_ashrrev_i32_e32 v1, 31, v0
	v_lshlrev_b64 v[4:5], 8, v[0:1]
	v_lshl_add_u64 v[6:7], s[34:35], 0, v[4:5]
	v_lshl_add_u64 v[6:7], v[6:7], 0, s[16:17]
	v_lshl_add_u64 v[4:5], s[38:39], 0, v[4:5]
	v_cvt_pk_bf16_f32 v0, v132, v133
	v_lshl_add_u64 v[6:7], v[6:7], 0, v[168:169]
	v_lshl_add_u64 v[4:5], v[4:5], 0, s[16:17]
	v_cvt_pk_bf16_f32 v1, v134, v135
	v_cvt_pk_bf16_f32 v2, v128, v129
	v_cvt_pk_bf16_f32 v3, v130, v131
	global_store_dwordx4 v[6:7], v[0:3], off nt
	v_lshl_add_u64 v[4:5], v[4:5], 0, v[168:169]
	s_nop 0
	v_cvt_pk_bf16_f32 v0, v100, v101
	v_cvt_pk_bf16_f32 v1, v102, v103
	v_cvt_pk_bf16_f32 v2, v96, v97
	v_cvt_pk_bf16_f32 v3, v98, v99
	global_store_dwordx4 v[4:5], v[0:3], off nt
	s_nop 1
	v_add_u32_e32 v0, 0x80, v171
	v_add_u32_e32 v0, s29, v0
	v_ashrrev_i32_e32 v1, 31, v0
	v_lshlrev_b64 v[4:5], 8, v[0:1]
	v_lshl_add_u64 v[6:7], s[34:35], 0, v[4:5]
	v_lshl_add_u64 v[6:7], v[6:7], 0, s[16:17]
	v_lshl_add_u64 v[4:5], s[38:39], 0, v[4:5]
	v_cvt_pk_bf16_f32 v0, v92, v93
	v_lshl_add_u64 v[6:7], v[6:7], 0, v[168:169]
	v_lshl_add_u64 v[4:5], v[4:5], 0, s[16:17]
	v_cvt_pk_bf16_f32 v1, v94, v95
	v_cvt_pk_bf16_f32 v2, v88, v89
	v_cvt_pk_bf16_f32 v3, v90, v91
	global_store_dwordx4 v[6:7], v[0:3], off nt
	v_lshl_add_u64 v[4:5], v[4:5], 0, v[168:169]
	s_nop 0
	v_cvt_pk_bf16_f32 v0, v104, v105
	v_cvt_pk_bf16_f32 v1, v62, v63
	v_cvt_pk_bf16_f32 v2, v114, v115
	v_cvt_pk_bf16_f32 v3, v60, v61
	global_store_dwordx4 v[4:5], v[0:3], off nt
	s_nop 1
	v_add_u32_e32 v0, 0x90, v171
	v_add_u32_e32 v0, s29, v0
	v_ashrrev_i32_e32 v1, 31, v0
	v_lshlrev_b64 v[4:5], 8, v[0:1]
	v_lshl_add_u64 v[6:7], s[34:35], 0, v[4:5]
	v_lshl_add_u64 v[6:7], v[6:7], 0, s[16:17]
	v_lshl_add_u64 v[4:5], s[38:39], 0, v[4:5]
	v_cvt_pk_bf16_f32 v0, v84, v85
	v_lshl_add_u64 v[6:7], v[6:7], 0, v[168:169]
	v_lshl_add_u64 v[4:5], v[4:5], 0, s[16:17]
	v_cvt_pk_bf16_f32 v1, v86, v87
	v_cvt_pk_bf16_f32 v2, v80, v81
	v_cvt_pk_bf16_f32 v3, v82, v83
	global_store_dwordx4 v[6:7], v[0:3], off nt
	v_lshl_add_u64 v[4:5], v[4:5], 0, v[168:169]
	s_nop 0
	v_cvt_pk_bf16_f32 v0, v56, v57
	v_cvt_pk_bf16_f32 v1, v54, v55
	v_cvt_pk_bf16_f32 v2, v58, v59
	v_cvt_pk_bf16_f32 v3, v52, v53
	global_store_dwordx4 v[4:5], v[0:3], off nt
	s_nop 1
	v_add_u32_e32 v0, 0xa0, v171
	v_add_u32_e32 v0, s29, v0
	v_ashrrev_i32_e32 v1, 31, v0
	v_lshlrev_b64 v[4:5], 8, v[0:1]
	v_lshl_add_u64 v[6:7], s[34:35], 0, v[4:5]
	v_lshl_add_u64 v[6:7], v[6:7], 0, s[16:17]
	v_lshl_add_u64 v[4:5], s[38:39], 0, v[4:5]
	v_cvt_pk_bf16_f32 v0, v76, v77
	v_lshl_add_u64 v[6:7], v[6:7], 0, v[168:169]
	v_lshl_add_u64 v[4:5], v[4:5], 0, s[16:17]
	v_cvt_pk_bf16_f32 v1, v78, v79
	v_cvt_pk_bf16_f32 v2, v72, v73
	v_cvt_pk_bf16_f32 v3, v74, v75
	global_store_dwordx4 v[6:7], v[0:3], off nt
	v_lshl_add_u64 v[4:5], v[4:5], 0, v[168:169]
	s_nop 0
	v_cvt_pk_bf16_f32 v0, v48, v49
	v_cvt_pk_bf16_f32 v1, v46, v47
	v_cvt_pk_bf16_f32 v2, v50, v51
	v_cvt_pk_bf16_f32 v3, v44, v45
	global_store_dwordx4 v[4:5], v[0:3], off nt
	s_nop 1
	v_add_u32_e32 v0, 0xb0, v171
	v_add_u32_e32 v0, s29, v0
	v_ashrrev_i32_e32 v1, 31, v0
	v_lshlrev_b64 v[4:5], 8, v[0:1]
	v_lshl_add_u64 v[6:7], s[34:35], 0, v[4:5]
	v_lshl_add_u64 v[4:5], s[38:39], 0, v[4:5]
	v_lshl_add_u64 v[6:7], v[6:7], 0, s[16:17]
	v_lshl_add_u64 v[4:5], v[4:5], 0, s[16:17]
	v_cvt_pk_bf16_f32 v0, v68, v69
	v_cvt_pk_bf16_f32 v1, v70, v71
	v_cvt_pk_bf16_f32 v2, v64, v65
	v_cvt_pk_bf16_f32 v3, v66, v67
	v_lshl_add_u64 v[6:7], v[6:7], 0, v[168:169]
	v_lshl_add_u64 v[4:5], v[4:5], 0, v[168:169]
	global_store_dwordx4 v[6:7], v[0:3], off nt
	s_nop 1
	v_cvt_pk_bf16_f32 v0, v40, v41
	v_cvt_pk_bf16_f32 v1, v38, v39
	v_cvt_pk_bf16_f32 v2, v42, v43
	v_cvt_pk_bf16_f32 v3, v36, v37
	global_store_dwordx4 v[4:5], v[0:3], off nt
	s_cbranch_vccnz .LBB0_248
	s_waitcnt lgkmcnt(0)
	s_barrier
